# nt weight stores + gate/up loop placement + extra barrier pair so the two wave halves run their down-projection epilogues concurrently (loop placement preserved)
# baseline (speedup 1.0000x reference)
; template <class Epi, class Sched>
; __device__ __forceinline__ void gemm_phase(LAS unsigned char* lds, const int K, const Sched& S, const Epi& E) {
;     ...
;         E(acc, cur, wr, wc, fr, fq);
;         if (!has_next) break;
;         cur = nxt; cA = nA; cB = nB; ++ui;
;         E.init(acc, cur, wc, fq);
.LBB0_2610:
	s_or_b64 exec, exec, s[24:25]
	s_cmpk_lt_u32 s49, 0x100
	s_cbranch_scc1 .Lx2_dn
	s_barrier
.Lx2_dn:
	s_nop 0
	s_nop 0
	s_nop 0
	s_nop 0
	s_nop 0
	s_nop 0
	s_nop 0
	s_nop 0
	s_nop 0
	s_nop 0
	s_nop 0
	s_nop 0
	s_nop 0
	s_and_b64 vcc, exec, s[12:13]
	s_mov_b32 s14, s60
	s_mov_b32 s62, s61
	s_mov_b64 s[22:23], s[10:11]
	s_cbranch_vccnz .LBB0_2666

; template <class Epi, class Sched>
; __device__ __forceinline__ void gemm_phase(LAS unsigned char* lds, const int K, const Sched& S, const Epi& E) {
;     ...
;         E(acc, cur, wr, wc, fr, fq);
;         if (!has_next) break;
;         cur = nxt; cA = nA; cB = nB; ++ui;
;         E.init(acc, cur, wc, fq);
.LBB0_2618:
	s_cmpk_gt_u32 s49, 0xff
	s_cbranch_scc1 .Lx1_dn
	s_barrier

; #define G8_WAIT_V(n) asm volatile("s_waitcnt vmcnt(" #n ")" ::: "memory")
; #define G8_BAR __builtin_amdgcn_s_barrier()
; template <class Epi, class Sched>
; __device__ __forceinline__ void gemm_phase(LAS unsigned char* lds, const int K, const Sched& S, const Epi& E) {
;     ...
;     G8_WAIT_V(0);
;     if (wr == 0) G8_BAR;
;     G8_BAR;
.LBB0_2666:
	s_nop 0
	s_nop 0
	s_nop 0
	s_nop 0
	s_nop 0
	s_nop 0
	s_nop 0
	s_nop 0
	s_nop 0
	s_nop 0
	s_nop 0
	s_nop 0
	s_nop 0
	s_waitcnt vmcnt(0)
	s_cmpk_gt_u32 s49, 0xff
	s_cbranch_scc1 .LBB0_2668
	s_barrier
